# gate-tile stores of the input projection as sc1 nt (write-through, streaming) instead of nt
# speedup vs baseline: 1.0098x; 1.0009x over previous
.Lpj_sigm:
	v_pk_mul_f32 v[126:127], v[126:127], v[136:137] op_sel_hi:[1,0]
	v_pk_mul_f32 v[128:129], v[128:129], v[136:137] op_sel_hi:[1,0]
	v_pk_mul_f32 v[122:123], v[122:123], v[136:137] op_sel_hi:[1,0]
	v_pk_mul_f32 v[124:125], v[124:125], v[136:137] op_sel_hi:[1,0]
	v_pk_mul_f32 v[144:145], v[126:127], v[186:187]
	v_pk_mul_f32 v[146:147], v[128:129], v[186:187]
	v_pk_mul_f32 v[148:149], v[122:123], v[186:187]
	v_pk_mul_f32 v[150:151], v[124:125], v[186:187]
	v_exp_f32_e32 v144, v144
	v_exp_f32_e32 v145, v145
	v_exp_f32_e32 v146, v146
	v_exp_f32_e32 v147, v147
	v_exp_f32_e32 v148, v148
	v_exp_f32_e32 v149, v149
	v_exp_f32_e32 v150, v150
	v_exp_f32_e32 v151, v151
	s_nop 0
	v_pk_add_f32 v[144:145], v[144:145], v[184:185]
	v_pk_add_f32 v[146:147], v[146:147], v[184:185]
	v_pk_add_f32 v[148:149], v[148:149], v[184:185]
	v_pk_add_f32 v[150:151], v[150:151], v[184:185]
	v_rcp_f32_e32 v144, v144
	v_rcp_f32_e32 v145, v145
	v_rcp_f32_e32 v146, v146
	v_rcp_f32_e32 v147, v147
	v_rcp_f32_e32 v148, v148
	v_rcp_f32_e32 v149, v149
	v_rcp_f32_e32 v150, v150
	v_rcp_f32_e32 v151, v151
	s_nop 0
	v_cvt_pk_bf16_f32 v126, v144, v145
	v_cvt_pk_bf16_f32 v127, v146, v147
	v_cvt_pk_bf16_f32 v128, v148, v149
	v_cvt_pk_bf16_f32 v129, v150, v151
	v_pk_mul_f32 v[118:119], v[118:119], v[136:137] op_sel_hi:[1,0]
	v_pk_mul_f32 v[120:121], v[120:121], v[136:137] op_sel_hi:[1,0]
	v_pk_mul_f32 v[114:115], v[114:115], v[136:137] op_sel_hi:[1,0]
	v_pk_mul_f32 v[116:117], v[116:117], v[136:137] op_sel_hi:[1,0]
	v_pk_mul_f32 v[144:145], v[118:119], v[186:187]
	v_pk_mul_f32 v[146:147], v[120:121], v[186:187]
	v_pk_mul_f32 v[148:149], v[114:115], v[186:187]
	v_pk_mul_f32 v[150:151], v[116:117], v[186:187]
	v_exp_f32_e32 v144, v144
	v_exp_f32_e32 v145, v145
	v_exp_f32_e32 v146, v146
	v_exp_f32_e32 v147, v147
	v_exp_f32_e32 v148, v148
	v_exp_f32_e32 v149, v149
	v_exp_f32_e32 v150, v150
	v_exp_f32_e32 v151, v151
	s_nop 0
	v_pk_add_f32 v[144:145], v[144:145], v[184:185]
	v_pk_add_f32 v[146:147], v[146:147], v[184:185]
	v_pk_add_f32 v[148:149], v[148:149], v[184:185]
	v_pk_add_f32 v[150:151], v[150:151], v[184:185]
	v_rcp_f32_e32 v144, v144
	v_rcp_f32_e32 v145, v145
	v_rcp_f32_e32 v146, v146
	v_rcp_f32_e32 v147, v147
	v_rcp_f32_e32 v148, v148
	v_rcp_f32_e32 v149, v149
	v_rcp_f32_e32 v150, v150
	v_rcp_f32_e32 v151, v151
	s_nop 0
	v_cvt_pk_bf16_f32 v118, v144, v145
	v_cvt_pk_bf16_f32 v119, v146, v147
	v_cvt_pk_bf16_f32 v120, v148, v149
	v_cvt_pk_bf16_f32 v121, v150, v151
	v_mov_b32_e32 v158, v118
	v_mov_b32_e32 v159, v119
	v_mov_b32_e32 v160, v120
	v_mov_b32_e32 v161, v121
	v_mov_b32_dpp v118, v126 row_shl:8 row_mask:0xf bank_mask:0x3
	v_mov_b32_dpp v119, v127 row_shl:8 row_mask:0xf bank_mask:0x3
	v_mov_b32_dpp v120, v128 row_shl:8 row_mask:0xf bank_mask:0x3
	v_mov_b32_dpp v121, v129 row_shl:8 row_mask:0xf bank_mask:0x3
	v_mov_b32_dpp v126, v158 row_shr:8 row_mask:0xf bank_mask:0xc
	v_mov_b32_dpp v127, v159 row_shr:8 row_mask:0xf bank_mask:0xc
	v_mov_b32_dpp v128, v160 row_shr:8 row_mask:0xf bank_mask:0xc
	v_mov_b32_dpp v129, v161 row_shr:8 row_mask:0xf bank_mask:0xc
	s_mul_i32 s28, s22, 0
	v_lshl_add_u64 v[180:181], s[28:29], 0, v[178:179]
	global_store_dwordx4 v[180:181], v[126:129], off sc1 nt
	s_mul_i32 s28, s22, 8
	v_lshl_add_u64 v[180:181], s[28:29], 0, v[178:179]
	global_store_dwordx4 v[180:181], v[118:121], off sc1 nt
	v_pk_mul_f32 v[110:111], v[110:111], v[136:137] op_sel:[0,1] op_sel_hi:[1,1]
	v_pk_mul_f32 v[112:113], v[112:113], v[136:137] op_sel:[0,1] op_sel_hi:[1,1]
	v_pk_mul_f32 v[106:107], v[106:107], v[136:137] op_sel:[0,1] op_sel_hi:[1,1]
	v_pk_mul_f32 v[108:109], v[108:109], v[136:137] op_sel:[0,1] op_sel_hi:[1,1]
	v_pk_mul_f32 v[144:145], v[110:111], v[186:187]
	v_pk_mul_f32 v[146:147], v[112:113], v[186:187]
	v_pk_mul_f32 v[148:149], v[106:107], v[186:187]
	v_pk_mul_f32 v[150:151], v[108:109], v[186:187]
	v_exp_f32_e32 v144, v144
	v_exp_f32_e32 v145, v145
	v_exp_f32_e32 v146, v146
	v_exp_f32_e32 v147, v147
	v_exp_f32_e32 v148, v148
	v_exp_f32_e32 v149, v149
	v_exp_f32_e32 v150, v150
	v_exp_f32_e32 v151, v151
	s_nop 0
	v_pk_add_f32 v[144:145], v[144:145], v[184:185]
	v_pk_add_f32 v[146:147], v[146:147], v[184:185]
	v_pk_add_f32 v[148:149], v[148:149], v[184:185]
	v_pk_add_f32 v[150:151], v[150:151], v[184:185]
	v_rcp_f32_e32 v144, v144
	v_rcp_f32_e32 v145, v145
	v_rcp_f32_e32 v146, v146
	v_rcp_f32_e32 v147, v147
	v_rcp_f32_e32 v148, v148
	v_rcp_f32_e32 v149, v149
	v_rcp_f32_e32 v150, v150
	v_rcp_f32_e32 v151, v151
	s_nop 0
	v_cvt_pk_bf16_f32 v110, v144, v145
	v_cvt_pk_bf16_f32 v111, v146, v147
	v_cvt_pk_bf16_f32 v112, v148, v149
	v_cvt_pk_bf16_f32 v113, v150, v151
	v_pk_mul_f32 v[102:103], v[102:103], v[136:137] op_sel:[0,1] op_sel_hi:[1,1]
	v_pk_mul_f32 v[104:105], v[104:105], v[136:137] op_sel:[0,1] op_sel_hi:[1,1]
	v_pk_mul_f32 v[98:99], v[98:99], v[136:137] op_sel:[0,1] op_sel_hi:[1,1]
	v_pk_mul_f32 v[100:101], v[100:101], v[136:137] op_sel:[0,1] op_sel_hi:[1,1]
	v_pk_mul_f32 v[144:145], v[102:103], v[186:187]
	v_pk_mul_f32 v[146:147], v[104:105], v[186:187]
	v_pk_mul_f32 v[148:149], v[98:99], v[186:187]
	v_pk_mul_f32 v[150:151], v[100:101], v[186:187]
	v_exp_f32_e32 v144, v144
	v_exp_f32_e32 v145, v145
	v_exp_f32_e32 v146, v146
	v_exp_f32_e32 v147, v147
	v_exp_f32_e32 v148, v148
	v_exp_f32_e32 v149, v149
	v_exp_f32_e32 v150, v150
	v_exp_f32_e32 v151, v151
	s_nop 0
	v_pk_add_f32 v[144:145], v[144:145], v[184:185]
	v_pk_add_f32 v[146:147], v[146:147], v[184:185]
	v_pk_add_f32 v[148:149], v[148:149], v[184:185]
	v_pk_add_f32 v[150:151], v[150:151], v[184:185]
	v_rcp_f32_e32 v144, v144
	v_rcp_f32_e32 v145, v145
	v_rcp_f32_e32 v146, v146
	v_rcp_f32_e32 v147, v147
	v_rcp_f32_e32 v148, v148
	v_rcp_f32_e32 v149, v149
	v_rcp_f32_e32 v150, v150
	v_rcp_f32_e32 v151, v151
	s_nop 0
	v_cvt_pk_bf16_f32 v102, v144, v145
	v_cvt_pk_bf16_f32 v103, v146, v147
	v_cvt_pk_bf16_f32 v104, v148, v149
	v_cvt_pk_bf16_f32 v105, v150, v151
	v_mov_b32_e32 v158, v102
	v_mov_b32_e32 v159, v103
	v_mov_b32_e32 v160, v104
	v_mov_b32_e32 v161, v105
	v_mov_b32_dpp v102, v110 row_shl:8 row_mask:0xf bank_mask:0x3
	v_mov_b32_dpp v103, v111 row_shl:8 row_mask:0xf bank_mask:0x3
	v_mov_b32_dpp v104, v112 row_shl:8 row_mask:0xf bank_mask:0x3
	v_mov_b32_dpp v105, v113 row_shl:8 row_mask:0xf bank_mask:0x3
	v_mov_b32_dpp v110, v158 row_shr:8 row_mask:0xf bank_mask:0xc
	v_mov_b32_dpp v111, v159 row_shr:8 row_mask:0xf bank_mask:0xc
	v_mov_b32_dpp v112, v160 row_shr:8 row_mask:0xf bank_mask:0xc
	v_mov_b32_dpp v113, v161 row_shr:8 row_mask:0xf bank_mask:0xc
	s_mul_i32 s28, s22, 16
	v_lshl_add_u64 v[180:181], s[28:29], 0, v[178:179]
	global_store_dwordx4 v[180:181], v[110:113], off sc1 nt
	s_mul_i32 s28, s22, 24
	v_lshl_add_u64 v[180:181], s[28:29], 0, v[178:179]
	global_store_dwordx4 v[180:181], v[102:105], off sc1 nt
	v_pk_mul_f32 v[94:95], v[94:95], v[138:139] op_sel_hi:[1,0]
	v_pk_mul_f32 v[96:97], v[96:97], v[138:139] op_sel_hi:[1,0]
	v_pk_mul_f32 v[90:91], v[90:91], v[138:139] op_sel_hi:[1,0]
	v_pk_mul_f32 v[92:93], v[92:93], v[138:139] op_sel_hi:[1,0]
	v_pk_mul_f32 v[144:145], v[94:95], v[186:187]
	v_pk_mul_f32 v[146:147], v[96:97], v[186:187]
	v_pk_mul_f32 v[148:149], v[90:91], v[186:187]
	v_pk_mul_f32 v[150:151], v[92:93], v[186:187]
	v_exp_f32_e32 v144, v144
	v_exp_f32_e32 v145, v145
	v_exp_f32_e32 v146, v146
	v_exp_f32_e32 v147, v147
	v_exp_f32_e32 v148, v148
	v_exp_f32_e32 v149, v149
	v_exp_f32_e32 v150, v150
	v_exp_f32_e32 v151, v151
	s_nop 0
	v_pk_add_f32 v[144:145], v[144:145], v[184:185]
	v_pk_add_f32 v[146:147], v[146:147], v[184:185]
	v_pk_add_f32 v[148:149], v[148:149], v[184:185]
	v_pk_add_f32 v[150:151], v[150:151], v[184:185]
	v_rcp_f32_e32 v144, v144
	v_rcp_f32_e32 v145, v145
	v_rcp_f32_e32 v146, v146
	v_rcp_f32_e32 v147, v147
	v_rcp_f32_e32 v148, v148
	v_rcp_f32_e32 v149, v149
	v_rcp_f32_e32 v150, v150
	v_rcp_f32_e32 v151, v151
	s_nop 0
	v_cvt_pk_bf16_f32 v94, v144, v145
	v_cvt_pk_bf16_f32 v95, v146, v147
	v_cvt_pk_bf16_f32 v96, v148, v149
	v_cvt_pk_bf16_f32 v97, v150, v151
	v_pk_mul_f32 v[86:87], v[86:87], v[138:139] op_sel_hi:[1,0]
	v_pk_mul_f32 v[88:89], v[88:89], v[138:139] op_sel_hi:[1,0]
	v_pk_mul_f32 v[82:83], v[82:83], v[138:139] op_sel_hi:[1,0]
	v_pk_mul_f32 v[84:85], v[84:85], v[138:139] op_sel_hi:[1,0]
	v_pk_mul_f32 v[144:145], v[86:87], v[186:187]
	v_pk_mul_f32 v[146:147], v[88:89], v[186:187]
	v_pk_mul_f32 v[148:149], v[82:83], v[186:187]
	v_pk_mul_f32 v[150:151], v[84:85], v[186:187]
	v_exp_f32_e32 v144, v144
	v_exp_f32_e32 v145, v145
	v_exp_f32_e32 v146, v146
	v_exp_f32_e32 v147, v147
	v_exp_f32_e32 v148, v148
	v_exp_f32_e32 v149, v149
	v_exp_f32_e32 v150, v150
	v_exp_f32_e32 v151, v151
	s_nop 0
	v_pk_add_f32 v[144:145], v[144:145], v[184:185]
	v_pk_add_f32 v[146:147], v[146:147], v[184:185]
	v_pk_add_f32 v[148:149], v[148:149], v[184:185]
	v_pk_add_f32 v[150:151], v[150:151], v[184:185]
	v_rcp_f32_e32 v144, v144
	v_rcp_f32_e32 v145, v145
	v_rcp_f32_e32 v146, v146
	v_rcp_f32_e32 v147, v147
	v_rcp_f32_e32 v148, v148
	v_rcp_f32_e32 v149, v149
	v_rcp_f32_e32 v150, v150
	v_rcp_f32_e32 v151, v151
	s_nop 0
	v_cvt_pk_bf16_f32 v86, v144, v145
	v_cvt_pk_bf16_f32 v87, v146, v147
	v_cvt_pk_bf16_f32 v88, v148, v149
	v_cvt_pk_bf16_f32 v89, v150, v151
	v_mov_b32_e32 v158, v86
	v_mov_b32_e32 v159, v87
	v_mov_b32_e32 v160, v88
	v_mov_b32_e32 v161, v89
	v_mov_b32_dpp v86, v94 row_shl:8 row_mask:0xf bank_mask:0x3
	v_mov_b32_dpp v87, v95 row_shl:8 row_mask:0xf bank_mask:0x3
	v_mov_b32_dpp v88, v96 row_shl:8 row_mask:0xf bank_mask:0x3
	v_mov_b32_dpp v89, v97 row_shl:8 row_mask:0xf bank_mask:0x3
	v_mov_b32_dpp v94, v158 row_shr:8 row_mask:0xf bank_mask:0xc
	v_mov_b32_dpp v95, v159 row_shr:8 row_mask:0xf bank_mask:0xc
	v_mov_b32_dpp v96, v160 row_shr:8 row_mask:0xf bank_mask:0xc
	v_mov_b32_dpp v97, v161 row_shr:8 row_mask:0xf bank_mask:0xc
	s_mul_i32 s28, s22, 32
	v_lshl_add_u64 v[180:181], s[28:29], 0, v[178:179]
	global_store_dwordx4 v[180:181], v[94:97], off sc1 nt
	s_mul_i32 s28, s22, 40
	v_lshl_add_u64 v[180:181], s[28:29], 0, v[178:179]
	global_store_dwordx4 v[180:181], v[86:89], off sc1 nt
	v_pk_mul_f32 v[78:79], v[78:79], v[138:139] op_sel:[0,1] op_sel_hi:[1,1]
	v_pk_mul_f32 v[80:81], v[80:81], v[138:139] op_sel:[0,1] op_sel_hi:[1,1]
	v_pk_mul_f32 v[74:75], v[74:75], v[138:139] op_sel:[0,1] op_sel_hi:[1,1]
	v_pk_mul_f32 v[76:77], v[76:77], v[138:139] op_sel:[0,1] op_sel_hi:[1,1]
	v_pk_mul_f32 v[144:145], v[78:79], v[186:187]
	v_pk_mul_f32 v[146:147], v[80:81], v[186:187]
	v_pk_mul_f32 v[148:149], v[74:75], v[186:187]
	v_pk_mul_f32 v[150:151], v[76:77], v[186:187]
	v_exp_f32_e32 v144, v144
	v_exp_f32_e32 v145, v145
	v_exp_f32_e32 v146, v146
	v_exp_f32_e32 v147, v147
	v_exp_f32_e32 v148, v148
	v_exp_f32_e32 v149, v149
	v_exp_f32_e32 v150, v150
	v_exp_f32_e32 v151, v151
	s_nop 0
	v_pk_add_f32 v[144:145], v[144:145], v[184:185]
	v_pk_add_f32 v[146:147], v[146:147], v[184:185]
	v_pk_add_f32 v[148:149], v[148:149], v[184:185]
	v_pk_add_f32 v[150:151], v[150:151], v[184:185]
	v_rcp_f32_e32 v144, v144
	v_rcp_f32_e32 v145, v145
	v_rcp_f32_e32 v146, v146
	v_rcp_f32_e32 v147, v147
	v_rcp_f32_e32 v148, v148
	v_rcp_f32_e32 v149, v149
	v_rcp_f32_e32 v150, v150
	v_rcp_f32_e32 v151, v151
	s_nop 0
	v_cvt_pk_bf16_f32 v78, v144, v145
	v_cvt_pk_bf16_f32 v79, v146, v147
	v_cvt_pk_bf16_f32 v80, v148, v149
	v_cvt_pk_bf16_f32 v81, v150, v151
	v_pk_mul_f32 v[70:71], v[70:71], v[138:139] op_sel:[0,1] op_sel_hi:[1,1]
	v_pk_mul_f32 v[72:73], v[72:73], v[138:139] op_sel:[0,1] op_sel_hi:[1,1]
	v_pk_mul_f32 v[66:67], v[66:67], v[138:139] op_sel:[0,1] op_sel_hi:[1,1]
	v_pk_mul_f32 v[68:69], v[68:69], v[138:139] op_sel:[0,1] op_sel_hi:[1,1]
	v_pk_mul_f32 v[144:145], v[70:71], v[186:187]
	v_pk_mul_f32 v[146:147], v[72:73], v[186:187]
	v_pk_mul_f32 v[148:149], v[66:67], v[186:187]
	v_pk_mul_f32 v[150:151], v[68:69], v[186:187]
	v_exp_f32_e32 v144, v144
	v_exp_f32_e32 v145, v145
	v_exp_f32_e32 v146, v146
	v_exp_f32_e32 v147, v147
	v_exp_f32_e32 v148, v148
	v_exp_f32_e32 v149, v149
	v_exp_f32_e32 v150, v150
	v_exp_f32_e32 v151, v151
	s_nop 0
	v_pk_add_f32 v[144:145], v[144:145], v[184:185]
	v_pk_add_f32 v[146:147], v[146:147], v[184:185]
	v_pk_add_f32 v[148:149], v[148:149], v[184:185]
	v_pk_add_f32 v[150:151], v[150:151], v[184:185]
	v_rcp_f32_e32 v144, v144
	v_rcp_f32_e32 v145, v145
	v_rcp_f32_e32 v146, v146
	v_rcp_f32_e32 v147, v147
	v_rcp_f32_e32 v148, v148
	v_rcp_f32_e32 v149, v149
	v_rcp_f32_e32 v150, v150
	v_rcp_f32_e32 v151, v151
	s_nop 0
	v_cvt_pk_bf16_f32 v70, v144, v145
	v_cvt_pk_bf16_f32 v71, v146, v147
	v_cvt_pk_bf16_f32 v72, v148, v149
	v_cvt_pk_bf16_f32 v73, v150, v151
	v_mov_b32_e32 v158, v70
	v_mov_b32_e32 v159, v71
	v_mov_b32_e32 v160, v72
	v_mov_b32_e32 v161, v73
	v_mov_b32_dpp v70, v78 row_shl:8 row_mask:0xf bank_mask:0x3
	v_mov_b32_dpp v71, v79 row_shl:8 row_mask:0xf bank_mask:0x3
	v_mov_b32_dpp v72, v80 row_shl:8 row_mask:0xf bank_mask:0x3
	v_mov_b32_dpp v73, v81 row_shl:8 row_mask:0xf bank_mask:0x3
	v_mov_b32_dpp v78, v158 row_shr:8 row_mask:0xf bank_mask:0xc
	v_mov_b32_dpp v79, v159 row_shr:8 row_mask:0xf bank_mask:0xc
	v_mov_b32_dpp v80, v160 row_shr:8 row_mask:0xf bank_mask:0xc
	v_mov_b32_dpp v81, v161 row_shr:8 row_mask:0xf bank_mask:0xc
	s_mul_i32 s28, s22, 48
	v_lshl_add_u64 v[180:181], s[28:29], 0, v[178:179]
	global_store_dwordx4 v[180:181], v[78:81], off sc1 nt
	s_mul_i32 s28, s22, 56
	v_lshl_add_u64 v[180:181], s[28:29], 0, v[178:179]
	global_store_dwordx4 v[180:181], v[70:73], off sc1 nt
	v_pk_mul_f32 v[62:63], v[62:63], v[140:141] op_sel_hi:[1,0]
	v_pk_mul_f32 v[64:65], v[64:65], v[140:141] op_sel_hi:[1,0]
	v_pk_mul_f32 v[58:59], v[58:59], v[140:141] op_sel_hi:[1,0]
	v_pk_mul_f32 v[60:61], v[60:61], v[140:141] op_sel_hi:[1,0]
	v_pk_mul_f32 v[144:145], v[62:63], v[186:187]
	v_pk_mul_f32 v[146:147], v[64:65], v[186:187]
	v_pk_mul_f32 v[148:149], v[58:59], v[186:187]
	v_pk_mul_f32 v[150:151], v[60:61], v[186:187]
	v_exp_f32_e32 v144, v144
	v_exp_f32_e32 v145, v145
	v_exp_f32_e32 v146, v146
	v_exp_f32_e32 v147, v147
	v_exp_f32_e32 v148, v148
	v_exp_f32_e32 v149, v149
	v_exp_f32_e32 v150, v150
	v_exp_f32_e32 v151, v151
	s_nop 0
	v_pk_add_f32 v[144:145], v[144:145], v[184:185]
	v_pk_add_f32 v[146:147], v[146:147], v[184:185]
	v_pk_add_f32 v[148:149], v[148:149], v[184:185]
	v_pk_add_f32 v[150:151], v[150:151], v[184:185]
	v_rcp_f32_e32 v144, v144
	v_rcp_f32_e32 v145, v145
	v_rcp_f32_e32 v146, v146
	v_rcp_f32_e32 v147, v147
	v_rcp_f32_e32 v148, v148
	v_rcp_f32_e32 v149, v149
	v_rcp_f32_e32 v150, v150
	v_rcp_f32_e32 v151, v151
	s_nop 0
	v_cvt_pk_bf16_f32 v62, v144, v145
	v_cvt_pk_bf16_f32 v63, v146, v147
	v_cvt_pk_bf16_f32 v64, v148, v149
	v_cvt_pk_bf16_f32 v65, v150, v151
	v_pk_mul_f32 v[54:55], v[54:55], v[140:141] op_sel_hi:[1,0]
	v_pk_mul_f32 v[56:57], v[56:57], v[140:141] op_sel_hi:[1,0]
	v_pk_mul_f32 v[50:51], v[50:51], v[140:141] op_sel_hi:[1,0]
	v_pk_mul_f32 v[52:53], v[52:53], v[140:141] op_sel_hi:[1,0]
	v_pk_mul_f32 v[144:145], v[54:55], v[186:187]
	v_pk_mul_f32 v[146:147], v[56:57], v[186:187]
	v_pk_mul_f32 v[148:149], v[50:51], v[186:187]
	v_pk_mul_f32 v[150:151], v[52:53], v[186:187]
	v_exp_f32_e32 v144, v144
	v_exp_f32_e32 v145, v145
	v_exp_f32_e32 v146, v146
	v_exp_f32_e32 v147, v147
	v_exp_f32_e32 v148, v148
	v_exp_f32_e32 v149, v149
	v_exp_f32_e32 v150, v150
	v_exp_f32_e32 v151, v151
	s_nop 0
	v_pk_add_f32 v[144:145], v[144:145], v[184:185]
	v_pk_add_f32 v[146:147], v[146:147], v[184:185]
	v_pk_add_f32 v[148:149], v[148:149], v[184:185]
	v_pk_add_f32 v[150:151], v[150:151], v[184:185]
	v_rcp_f32_e32 v144, v144
	v_rcp_f32_e32 v145, v145
	v_rcp_f32_e32 v146, v146
	v_rcp_f32_e32 v147, v147
	v_rcp_f32_e32 v148, v148
	v_rcp_f32_e32 v149, v149
	v_rcp_f32_e32 v150, v150
	v_rcp_f32_e32 v151, v151
	s_nop 0
	v_cvt_pk_bf16_f32 v54, v144, v145
	v_cvt_pk_bf16_f32 v55, v146, v147
	v_cvt_pk_bf16_f32 v56, v148, v149
	v_cvt_pk_bf16_f32 v57, v150, v151
	v_mov_b32_e32 v158, v54
	v_mov_b32_e32 v159, v55
	v_mov_b32_e32 v160, v56
	v_mov_b32_e32 v161, v57
	v_mov_b32_dpp v54, v62 row_shl:8 row_mask:0xf bank_mask:0x3
	v_mov_b32_dpp v55, v63 row_shl:8 row_mask:0xf bank_mask:0x3
	v_mov_b32_dpp v56, v64 row_shl:8 row_mask:0xf bank_mask:0x3
	v_mov_b32_dpp v57, v65 row_shl:8 row_mask:0xf bank_mask:0x3
	v_mov_b32_dpp v62, v158 row_shr:8 row_mask:0xf bank_mask:0xc
	v_mov_b32_dpp v63, v159 row_shr:8 row_mask:0xf bank_mask:0xc
	v_mov_b32_dpp v64, v160 row_shr:8 row_mask:0xf bank_mask:0xc
	v_mov_b32_dpp v65, v161 row_shr:8 row_mask:0xf bank_mask:0xc
	s_mul_i32 s28, s22, 128
	v_lshl_add_u64 v[180:181], s[28:29], 0, v[178:179]
	global_store_dwordx4 v[180:181], v[62:65], off sc1 nt
	s_mul_i32 s28, s22, 136
	v_lshl_add_u64 v[180:181], s[28:29], 0, v[178:179]
	global_store_dwordx4 v[180:181], v[54:57], off sc1 nt
	v_pk_mul_f32 v[46:47], v[46:47], v[140:141] op_sel:[0,1] op_sel_hi:[1,1]
	v_pk_mul_f32 v[48:49], v[48:49], v[140:141] op_sel:[0,1] op_sel_hi:[1,1]
	v_pk_mul_f32 v[42:43], v[42:43], v[140:141] op_sel:[0,1] op_sel_hi:[1,1]
	v_pk_mul_f32 v[44:45], v[44:45], v[140:141] op_sel:[0,1] op_sel_hi:[1,1]
	v_pk_mul_f32 v[144:145], v[46:47], v[186:187]
	v_pk_mul_f32 v[146:147], v[48:49], v[186:187]
	v_pk_mul_f32 v[148:149], v[42:43], v[186:187]
	v_pk_mul_f32 v[150:151], v[44:45], v[186:187]
	v_exp_f32_e32 v144, v144
	v_exp_f32_e32 v145, v145
	v_exp_f32_e32 v146, v146
	v_exp_f32_e32 v147, v147
	v_exp_f32_e32 v148, v148
	v_exp_f32_e32 v149, v149
	v_exp_f32_e32 v150, v150
	v_exp_f32_e32 v151, v151
	s_nop 0
	v_pk_add_f32 v[144:145], v[144:145], v[184:185]
	v_pk_add_f32 v[146:147], v[146:147], v[184:185]
	v_pk_add_f32 v[148:149], v[148:149], v[184:185]
	v_pk_add_f32 v[150:151], v[150:151], v[184:185]
	v_rcp_f32_e32 v144, v144
	v_rcp_f32_e32 v145, v145
	v_rcp_f32_e32 v146, v146
	v_rcp_f32_e32 v147, v147
	v_rcp_f32_e32 v148, v148
	v_rcp_f32_e32 v149, v149
	v_rcp_f32_e32 v150, v150
	v_rcp_f32_e32 v151, v151
	s_nop 0
	v_cvt_pk_bf16_f32 v46, v144, v145
	v_cvt_pk_bf16_f32 v47, v146, v147
	v_cvt_pk_bf16_f32 v48, v148, v149
	v_cvt_pk_bf16_f32 v49, v150, v151
	v_pk_mul_f32 v[38:39], v[38:39], v[140:141] op_sel:[0,1] op_sel_hi:[1,1]
	v_pk_mul_f32 v[40:41], v[40:41], v[140:141] op_sel:[0,1] op_sel_hi:[1,1]
	v_pk_mul_f32 v[34:35], v[34:35], v[140:141] op_sel:[0,1] op_sel_hi:[1,1]
	v_pk_mul_f32 v[36:37], v[36:37], v[140:141] op_sel:[0,1] op_sel_hi:[1,1]
	v_pk_mul_f32 v[144:145], v[38:39], v[186:187]
	v_pk_mul_f32 v[146:147], v[40:41], v[186:187]
	v_pk_mul_f32 v[148:149], v[34:35], v[186:187]
	v_pk_mul_f32 v[150:151], v[36:37], v[186:187]
	v_exp_f32_e32 v144, v144
	v_exp_f32_e32 v145, v145
	v_exp_f32_e32 v146, v146
	v_exp_f32_e32 v147, v147
	v_exp_f32_e32 v148, v148
	v_exp_f32_e32 v149, v149
	v_exp_f32_e32 v150, v150
	v_exp_f32_e32 v151, v151
	s_nop 0
	v_pk_add_f32 v[144:145], v[144:145], v[184:185]
	v_pk_add_f32 v[146:147], v[146:147], v[184:185]
	v_pk_add_f32 v[148:149], v[148:149], v[184:185]
	v_pk_add_f32 v[150:151], v[150:151], v[184:185]
	v_rcp_f32_e32 v144, v144
	v_rcp_f32_e32 v145, v145
	v_rcp_f32_e32 v146, v146
	v_rcp_f32_e32 v147, v147
	v_rcp_f32_e32 v148, v148
	v_rcp_f32_e32 v149, v149
	v_rcp_f32_e32 v150, v150
	v_rcp_f32_e32 v151, v151
	s_nop 0
	v_cvt_pk_bf16_f32 v38, v144, v145
	v_cvt_pk_bf16_f32 v39, v146, v147
	v_cvt_pk_bf16_f32 v40, v148, v149
	v_cvt_pk_bf16_f32 v41, v150, v151
	v_mov_b32_e32 v158, v38
	v_mov_b32_e32 v159, v39
	v_mov_b32_e32 v160, v40
	v_mov_b32_e32 v161, v41
	v_mov_b32_dpp v38, v46 row_shl:8 row_mask:0xf bank_mask:0x3
	v_mov_b32_dpp v39, v47 row_shl:8 row_mask:0xf bank_mask:0x3
	v_mov_b32_dpp v40, v48 row_shl:8 row_mask:0xf bank_mask:0x3
	v_mov_b32_dpp v41, v49 row_shl:8 row_mask:0xf bank_mask:0x3
	v_mov_b32_dpp v46, v158 row_shr:8 row_mask:0xf bank_mask:0xc
	v_mov_b32_dpp v47, v159 row_shr:8 row_mask:0xf bank_mask:0xc
	v_mov_b32_dpp v48, v160 row_shr:8 row_mask:0xf bank_mask:0xc
	v_mov_b32_dpp v49, v161 row_shr:8 row_mask:0xf bank_mask:0xc
	s_mul_i32 s28, s22, 144
	v_lshl_add_u64 v[180:181], s[28:29], 0, v[178:179]
	global_store_dwordx4 v[180:181], v[46:49], off sc1 nt
	s_mul_i32 s28, s22, 152
	v_lshl_add_u64 v[180:181], s[28:29], 0, v[178:179]
	global_store_dwordx4 v[180:181], v[38:41], off sc1 nt
	v_pk_mul_f32 v[30:31], v[30:31], v[142:143] op_sel_hi:[1,0]
	v_pk_mul_f32 v[32:33], v[32:33], v[142:143] op_sel_hi:[1,0]
	v_pk_mul_f32 v[26:27], v[26:27], v[142:143] op_sel_hi:[1,0]
	v_pk_mul_f32 v[28:29], v[28:29], v[142:143] op_sel_hi:[1,0]
	v_pk_mul_f32 v[144:145], v[30:31], v[186:187]
	v_pk_mul_f32 v[146:147], v[32:33], v[186:187]
	v_pk_mul_f32 v[148:149], v[26:27], v[186:187]
	v_pk_mul_f32 v[150:151], v[28:29], v[186:187]
	v_exp_f32_e32 v144, v144
	v_exp_f32_e32 v145, v145
	v_exp_f32_e32 v146, v146
	v_exp_f32_e32 v147, v147
	v_exp_f32_e32 v148, v148
	v_exp_f32_e32 v149, v149
	v_exp_f32_e32 v150, v150
	v_exp_f32_e32 v151, v151
	s_nop 0
	v_pk_add_f32 v[144:145], v[144:145], v[184:185]
	v_pk_add_f32 v[146:147], v[146:147], v[184:185]
	v_pk_add_f32 v[148:149], v[148:149], v[184:185]
	v_pk_add_f32 v[150:151], v[150:151], v[184:185]
	v_rcp_f32_e32 v144, v144
	v_rcp_f32_e32 v145, v145
	v_rcp_f32_e32 v146, v146
	v_rcp_f32_e32 v147, v147
	v_rcp_f32_e32 v148, v148
	v_rcp_f32_e32 v149, v149
	v_rcp_f32_e32 v150, v150
	v_rcp_f32_e32 v151, v151
	s_nop 0
	v_cvt_pk_bf16_f32 v30, v144, v145
	v_cvt_pk_bf16_f32 v31, v146, v147
	v_cvt_pk_bf16_f32 v32, v148, v149
	v_cvt_pk_bf16_f32 v33, v150, v151
	v_pk_mul_f32 v[22:23], v[22:23], v[142:143] op_sel_hi:[1,0]
	v_pk_mul_f32 v[24:25], v[24:25], v[142:143] op_sel_hi:[1,0]
	v_pk_mul_f32 v[18:19], v[18:19], v[142:143] op_sel_hi:[1,0]
	v_pk_mul_f32 v[20:21], v[20:21], v[142:143] op_sel_hi:[1,0]
	v_pk_mul_f32 v[144:145], v[22:23], v[186:187]
	v_pk_mul_f32 v[146:147], v[24:25], v[186:187]
	v_pk_mul_f32 v[148:149], v[18:19], v[186:187]
	v_pk_mul_f32 v[150:151], v[20:21], v[186:187]
	v_exp_f32_e32 v144, v144
	v_exp_f32_e32 v145, v145
	v_exp_f32_e32 v146, v146
	v_exp_f32_e32 v147, v147
	v_exp_f32_e32 v148, v148
	v_exp_f32_e32 v149, v149
	v_exp_f32_e32 v150, v150
	v_exp_f32_e32 v151, v151
	s_nop 0
	v_pk_add_f32 v[144:145], v[144:145], v[184:185]
	v_pk_add_f32 v[146:147], v[146:147], v[184:185]
	v_pk_add_f32 v[148:149], v[148:149], v[184:185]
	v_pk_add_f32 v[150:151], v[150:151], v[184:185]
	v_rcp_f32_e32 v144, v144
	v_rcp_f32_e32 v145, v145
	v_rcp_f32_e32 v146, v146
	v_rcp_f32_e32 v147, v147
	v_rcp_f32_e32 v148, v148
	v_rcp_f32_e32 v149, v149
	v_rcp_f32_e32 v150, v150
	v_rcp_f32_e32 v151, v151
	s_nop 0
	v_cvt_pk_bf16_f32 v22, v144, v145
	v_cvt_pk_bf16_f32 v23, v146, v147
	v_cvt_pk_bf16_f32 v24, v148, v149
	v_cvt_pk_bf16_f32 v25, v150, v151
	v_mov_b32_e32 v158, v22
	v_mov_b32_e32 v159, v23
	v_mov_b32_e32 v160, v24
	v_mov_b32_e32 v161, v25
	v_mov_b32_dpp v22, v30 row_shl:8 row_mask:0xf bank_mask:0x3
	v_mov_b32_dpp v23, v31 row_shl:8 row_mask:0xf bank_mask:0x3
	v_mov_b32_dpp v24, v32 row_shl:8 row_mask:0xf bank_mask:0x3
	v_mov_b32_dpp v25, v33 row_shl:8 row_mask:0xf bank_mask:0x3
	v_mov_b32_dpp v30, v158 row_shr:8 row_mask:0xf bank_mask:0xc
	v_mov_b32_dpp v31, v159 row_shr:8 row_mask:0xf bank_mask:0xc
	v_mov_b32_dpp v32, v160 row_shr:8 row_mask:0xf bank_mask:0xc
	v_mov_b32_dpp v33, v161 row_shr:8 row_mask:0xf bank_mask:0xc
	s_mul_i32 s28, s22, 160
	v_lshl_add_u64 v[180:181], s[28:29], 0, v[178:179]
	global_store_dwordx4 v[180:181], v[30:33], off sc1 nt
	s_mul_i32 s28, s22, 168
	v_lshl_add_u64 v[180:181], s[28:29], 0, v[178:179]
	global_store_dwordx4 v[180:181], v[22:25], off sc1 nt
	v_pk_mul_f32 v[14:15], v[14:15], v[142:143] op_sel:[0,1] op_sel_hi:[1,1]
	v_pk_mul_f32 v[16:17], v[16:17], v[142:143] op_sel:[0,1] op_sel_hi:[1,1]
	v_pk_mul_f32 v[10:11], v[10:11], v[142:143] op_sel:[0,1] op_sel_hi:[1,1]
	v_pk_mul_f32 v[12:13], v[12:13], v[142:143] op_sel:[0,1] op_sel_hi:[1,1]
	v_pk_mul_f32 v[144:145], v[14:15], v[186:187]
	v_pk_mul_f32 v[146:147], v[16:17], v[186:187]
	v_pk_mul_f32 v[148:149], v[10:11], v[186:187]
	v_pk_mul_f32 v[150:151], v[12:13], v[186:187]
	v_exp_f32_e32 v144, v144
	v_exp_f32_e32 v145, v145
	v_exp_f32_e32 v146, v146
	v_exp_f32_e32 v147, v147
	v_exp_f32_e32 v148, v148
	v_exp_f32_e32 v149, v149
	v_exp_f32_e32 v150, v150
	v_exp_f32_e32 v151, v151
	s_nop 0
	v_pk_add_f32 v[144:145], v[144:145], v[184:185]
	v_pk_add_f32 v[146:147], v[146:147], v[184:185]
	v_pk_add_f32 v[148:149], v[148:149], v[184:185]
	v_pk_add_f32 v[150:151], v[150:151], v[184:185]
	v_rcp_f32_e32 v144, v144
	v_rcp_f32_e32 v145, v145
	v_rcp_f32_e32 v146, v146
	v_rcp_f32_e32 v147, v147
	v_rcp_f32_e32 v148, v148
	v_rcp_f32_e32 v149, v149
	v_rcp_f32_e32 v150, v150
	v_rcp_f32_e32 v151, v151
	s_nop 0
	v_cvt_pk_bf16_f32 v14, v144, v145
	v_cvt_pk_bf16_f32 v15, v146, v147
	v_cvt_pk_bf16_f32 v16, v148, v149
	v_cvt_pk_bf16_f32 v17, v150, v151
	v_pk_mul_f32 v[6:7], v[6:7], v[142:143] op_sel:[0,1] op_sel_hi:[1,1]
	v_pk_mul_f32 v[8:9], v[8:9], v[142:143] op_sel:[0,1] op_sel_hi:[1,1]
	v_pk_mul_f32 v[2:3], v[2:3], v[142:143] op_sel:[0,1] op_sel_hi:[1,1]
	v_pk_mul_f32 v[4:5], v[4:5], v[142:143] op_sel:[0,1] op_sel_hi:[1,1]
	v_pk_mul_f32 v[144:145], v[6:7], v[186:187]
	v_pk_mul_f32 v[146:147], v[8:9], v[186:187]
	v_pk_mul_f32 v[148:149], v[2:3], v[186:187]
	v_pk_mul_f32 v[150:151], v[4:5], v[186:187]
	v_exp_f32_e32 v144, v144
	v_exp_f32_e32 v145, v145
	v_exp_f32_e32 v146, v146
	v_exp_f32_e32 v147, v147
	v_exp_f32_e32 v148, v148
	v_exp_f32_e32 v149, v149
	v_exp_f32_e32 v150, v150
	v_exp_f32_e32 v151, v151
	s_nop 0
	v_pk_add_f32 v[144:145], v[144:145], v[184:185]
	v_pk_add_f32 v[146:147], v[146:147], v[184:185]
	v_pk_add_f32 v[148:149], v[148:149], v[184:185]
	v_pk_add_f32 v[150:151], v[150:151], v[184:185]
	v_rcp_f32_e32 v144, v144
	v_rcp_f32_e32 v145, v145
	v_rcp_f32_e32 v146, v146
	v_rcp_f32_e32 v147, v147
	v_rcp_f32_e32 v148, v148
	v_rcp_f32_e32 v149, v149
	v_rcp_f32_e32 v150, v150
	v_rcp_f32_e32 v151, v151
	s_nop 0
	v_cvt_pk_bf16_f32 v6, v144, v145
	v_cvt_pk_bf16_f32 v7, v146, v147
	v_cvt_pk_bf16_f32 v8, v148, v149
	v_cvt_pk_bf16_f32 v9, v150, v151
	v_mov_b32_e32 v158, v6
	v_mov_b32_e32 v159, v7
	v_mov_b32_e32 v160, v8
	v_mov_b32_e32 v161, v9
	v_mov_b32_dpp v6, v14 row_shl:8 row_mask:0xf bank_mask:0x3
	v_mov_b32_dpp v7, v15 row_shl:8 row_mask:0xf bank_mask:0x3
	v_mov_b32_dpp v8, v16 row_shl:8 row_mask:0xf bank_mask:0x3
	v_mov_b32_dpp v9, v17 row_shl:8 row_mask:0xf bank_mask:0x3
	v_mov_b32_dpp v14, v158 row_shr:8 row_mask:0xf bank_mask:0xc
	v_mov_b32_dpp v15, v159 row_shr:8 row_mask:0xf bank_mask:0xc
	v_mov_b32_dpp v16, v160 row_shr:8 row_mask:0xf bank_mask:0xc
	v_mov_b32_dpp v17, v161 row_shr:8 row_mask:0xf bank_mask:0xc
	s_mul_i32 s28, s22, 176
	v_lshl_add_u64 v[180:181], s[28:29], 0, v[178:179]
	global_store_dwordx4 v[180:181], v[14:17], off sc1 nt
	s_mul_i32 s28, s22, 184
	v_lshl_add_u64 v[180:181], s[28:29], 0, v[178:179]
	global_store_dwordx4 v[180:181], v[6:9], off sc1 nt
